# P6 norm_mod_rows row-pair loop software-pipelined (next pair's loads issued at the top of the current pair; counted wait keeps the stores in flight)
# speedup vs baseline: 1.0070x; 1.0055x over previous
.LBB0_1011:
	s_waitcnt vmcnt(8)
	v_mov_b32_e32 v44, v102
	v_mov_b32_e32 v45, v103
	v_mov_b32_e32 v46, v104
	v_mov_b32_e32 v47, v105
	v_mov_b32_e32 v48, v106
	v_mov_b32_e32 v49, v107
	v_mov_b32_e32 v50, v108
	v_mov_b32_e32 v51, v109
	v_mov_b32_e32 v52, v110
	v_mov_b32_e32 v53, v111
	v_mov_b32_e32 v54, v112
	v_mov_b32_e32 v55, v113
	v_mov_b32_e32 v56, v114
	v_mov_b32_e32 v57, v115
	v_mov_b32_e32 v58, v116
	v_mov_b32_e32 v59, v117
	s_add_i32 s98, s4, 2
	s_cmp_lt_i32 s98, s3
	s_cbranch_scc0 .Lp6_nopf
	s_mov_b32 s100, 0xea101000
	s_mov_b32 s101, -1
	v_lshl_add_u64 v[120:121], v[42:43], 0, s[100:101]
	global_load_dwordx2 v[116:117], v[120:121], off offset:-3584
	global_load_dwordx2 v[114:115], v[120:121], off offset:-3072
	global_load_dwordx2 v[112:113], v[120:121], off offset:-2560
	global_load_dwordx2 v[110:111], v[120:121], off offset:-2048
	global_load_dwordx2 v[108:109], v[120:121], off offset:-1536
	global_load_dwordx2 v[106:107], v[120:121], off offset:-1024
	global_load_dwordx2 v[104:105], v[120:121], off offset:-512
	global_load_dwordx2 v[102:103], v[120:121], off
.Lp6_nopf:
	v_and_b32_e32 v83, 0xffff0000, v59
	v_lshlrev_b32_e32 v80, 16, v58
	v_and_b32_e32 v81, 0xffff0000, v58
	v_lshlrev_b32_e32 v82, 16, v59
	v_lshlrev_b32_e32 v67, 16, v52
	v_and_b32_e32 v65, 0xffff0000, v52
	v_lshlrev_b32_e32 v62, 16, v53
	v_and_b32_e32 v63, 0xffff0000, v53
	v_lshlrev_b32_e32 v58, 16, v50
	v_and_b32_e32 v59, 0xffff0000, v50
	v_lshlrev_b32_e32 v60, 16, v51
	v_and_b32_e32 v61, 0xffff0000, v51
	v_lshlrev_b32_e32 v50, 16, v46
	v_and_b32_e32 v51, 0xffff0000, v46
	v_lshlrev_b32_e32 v52, 16, v47
	v_and_b32_e32 v53, 0xffff0000, v47
	v_and_b32_e32 v47, 0xffff0000, v44
	v_mul_f32_e32 v46, v83, v83
	v_and_b32_e32 v87, 0xffff0000, v57
	v_and_b32_e32 v86, 0xffff0000, v56
	v_pk_fma_f32 v[90:91], v[82:83], v[82:83], v[46:47] op_sel_hi:[1,1,0]
	v_mul_f32_e32 v46, v81, v81
	v_lshlrev_b32_e32 v85, 16, v57
	v_lshlrev_b32_e32 v84, 16, v56
	v_pk_mul_f32 v[92:93], v[86:87], v[86:87]
	v_pk_fma_f32 v[94:95], v[80:81], v[80:81], v[46:47] op_sel_hi:[1,1,0]
	v_pk_fma_f32 v[92:93], v[84:85], v[84:85], v[92:93]
	v_mov_b32_e32 v66, v94
	v_mov_b32_e32 v96, v90
	v_mov_b32_e32 v97, v67
	v_lshlrev_b32_e32 v68, 16, v54
	v_and_b32_e32 v69, 0xffff0000, v54
	v_lshlrev_b32_e32 v56, 16, v48
	v_and_b32_e32 v54, 0xffff0000, v48
	v_mul_f32_e32 v48, v65, v65
	v_pk_add_f32 v[90:91], v[94:95], v[90:91]
	v_pk_mul_f32 v[94:95], v[66:67], v[96:97]
	v_pk_add_f32 v[92:93], v[92:93], v[92:93] op_sel:[0,1] op_sel_hi:[1,0]
	v_and_b32_e32 v89, 0xffff0000, v55
	v_mov_b32_e32 v91, v95
	v_mov_b32_e32 v93, v48
	v_mul_f32_e32 v46, v69, v69
	v_lshlrev_b32_e32 v88, 16, v55
	v_pk_add_f32 v[90:91], v[90:91], v[92:93]
	v_pk_fma_f32 v[92:93], v[68:69], v[68:69], v[46:47] op_sel_hi:[1,1,0]
	v_mul_f32_e32 v46, v89, v89
	v_mul_f32_e32 v64, v62, v62
	v_mul_f32_e32 v98, v63, v63
	v_pk_fma_f32 v[94:95], v[88:89], v[88:89], v[46:47] op_sel_hi:[1,1,0]
	v_mov_b32_e32 v93, v64
	v_mov_b32_e32 v95, v98
	v_pk_add_f32 v[92:93], v[92:93], v[94:95]
	v_mul_f32_e32 v46, v61, v61
	v_pk_add_f32 v[90:91], v[90:91], v[92:93]
	v_lshlrev_b32_e32 v57, 16, v49
	v_add_f32_e32 v48, v90, v91
	ds_bpermute_b32 v64, v1, v48
	v_pk_fma_f32 v[90:91], v[60:61], v[60:61], v[46:47] op_sel_hi:[1,1,0]
	v_mul_f32_e32 v46, v59, v59
	v_pk_fma_f32 v[94:95], v[58:59], v[58:59], v[46:47] op_sel_hi:[1,1,0]
	v_and_b32_e32 v55, 0xffff0000, v49
	s_waitcnt lgkmcnt(0)
	v_add_f32_e32 v48, v48, v64
	ds_bpermute_b32 v64, v70, v48
	v_lshlrev_b32_e32 v49, 16, v44
	v_mov_b32_e32 v96, v90
	v_mov_b32_e32 v97, v49
	v_pk_add_f32 v[90:91], v[94:95], v[90:91]
	s_waitcnt lgkmcnt(0)
	v_add_f32_e32 v64, v48, v64
	ds_bpermute_b32 v100, v71, v64
	v_mov_b32_e32 v48, v94
	v_pk_mul_f32 v[94:95], v[48:49], v[96:97]
	v_pk_mul_f32 v[92:93], v[54:55], v[54:55]
	v_mul_f32_e32 v66, v47, v47
	s_waitcnt lgkmcnt(0)
	v_add_f32_e32 v46, v64, v100
	ds_bpermute_b32 v64, v72, v46
	v_pk_fma_f32 v[92:93], v[56:57], v[56:57], v[92:93]
	v_mov_b32_e32 v91, v95
	v_pk_add_f32 v[92:93], v[92:93], v[92:93] op_sel:[0,1] op_sel_hi:[1,0]
	v_lshlrev_b32_e32 v44, 16, v45
	s_waitcnt lgkmcnt(0)
	v_add_f32_e32 v48, v46, v64
	ds_bpermute_b32 v64, v73, v48
	v_mov_b32_e32 v93, v66
	v_mul_f32_e32 v46, v51, v51
	v_pk_add_f32 v[90:91], v[90:91], v[92:93]
	v_pk_fma_f32 v[92:93], v[50:51], v[50:51], v[46:47] op_sel_hi:[1,1,0]
	s_waitcnt lgkmcnt(0)
	v_add_f32_e32 v48, v48, v64
	ds_bpermute_b32 v64, v74, v48
	v_mul_f32_e32 v46, v53, v53
	v_pk_fma_f32 v[94:95], v[52:53], v[52:53], v[46:47] op_sel_hi:[1,1,0]
	v_and_b32_e32 v45, 0xffff0000, v45
	v_mul_f32_e32 v98, v44, v44
	s_waitcnt lgkmcnt(0)
	v_add_f32_e32 v46, v48, v64
	v_fmamk_f32 v46, v46, 0x3a800000, v79
	v_mul_f32_e32 v48, 0x4b800000, v46
	v_cmp_gt_f32_e32 vcc, s5, v46
	v_mul_f32_e32 v99, v45, v45
	v_mov_b32_e32 v93, v98
	v_cndmask_b32_e32 v46, v46, v48, vcc
	v_rsq_f32_e32 v46, v46
	v_mov_b32_e32 v95, v99
	v_pk_add_f32 v[92:93], v[92:93], v[94:95]
	s_add_i32 s4, s4, 2
	v_pk_add_f32 v[90:91], v[90:91], v[92:93]
	v_mul_f32_e32 v64, 0x45800000, v46
	v_add_f32_e32 v48, v90, v91
	v_cndmask_b32_e32 v46, v46, v64, vcc
	ds_bpermute_b32 v64, v1, v48
	v_pk_mul_f32 v[80:81], v[46:47], v[80:81] op_sel_hi:[0,1]
	v_pk_mul_f32 v[82:83], v[46:47], v[82:83] op_sel_hi:[0,1]
	v_pk_fma_f32 v[80:81], v[18:19], v[80:81], v[2:3]
	v_pk_fma_f32 v[82:83], v[20:21], v[82:83], v[4:5]
	s_waitcnt lgkmcnt(0)
	v_add_f32_e32 v48, v48, v64
	ds_bpermute_b32 v64, v70, v48
	v_cvt_pk_bf16_f32 v80, v80, v81
	v_cvt_pk_bf16_f32 v81, v82, v83
	global_store_dwordx2 v[42:43], v[80:81], off offset:-3584
	v_mov_b32_e32 v80, v84
	s_waitcnt lgkmcnt(0)
	v_add_f32_e32 v48, v48, v64
	ds_bpermute_b32 v64, v71, v48
	v_mov_b32_e32 v81, v86
	v_pk_mul_f32 v[80:81], v[46:47], v[80:81] op_sel_hi:[0,1]
	v_mov_b32_e32 v86, v85
	v_pk_mul_f32 v[82:83], v[46:47], v[86:87] op_sel_hi:[0,1]
	s_waitcnt lgkmcnt(0)
	v_add_f32_e32 v48, v48, v64
	ds_bpermute_b32 v64, v72, v48
	v_pk_fma_f32 v[80:81], v[22:23], v[80:81], v[6:7]
	v_pk_fma_f32 v[82:83], v[24:25], v[82:83], v[8:9]
	v_cvt_pk_bf16_f32 v80, v80, v81
	v_pk_mul_f32 v[68:69], v[46:47], v[68:69] op_sel_hi:[0,1]
	s_waitcnt lgkmcnt(0)
	v_add_f32_e32 v48, v48, v64
	ds_bpermute_b32 v66, v73, v48
	v_cvt_pk_bf16_f32 v81, v82, v83
	v_mov_b32_e32 v64, v67
	global_store_dwordx2 v[42:43], v[80:81], off offset:-3072
	v_pk_mul_f32 v[80:81], v[46:47], v[88:89] op_sel_hi:[0,1]
	s_waitcnt lgkmcnt(0)
	v_add_f32_e32 v48, v48, v66
	ds_bpermute_b32 v66, v74, v48
	v_pk_mul_f32 v[64:65], v[46:47], v[64:65] op_sel_hi:[0,1]
	v_pk_mul_f32 v[62:63], v[46:47], v[62:63] op_sel_hi:[0,1]
	v_pk_fma_f32 v[68:69], v[26:27], v[68:69], v[10:11]
	v_pk_fma_f32 v[64:65], v[30:31], v[64:65], v[14:15]
	s_waitcnt lgkmcnt(0)
	v_add_f32_e32 v46, v48, v66
	v_fmamk_f32 v46, v46, 0x3a800000, v79
	v_mul_f32_e32 v48, 0x4b800000, v46
	v_cmp_gt_f32_e32 vcc, s5, v46
	v_pk_fma_f32 v[80:81], v[28:29], v[80:81], v[12:13]
	v_cvt_pk_bf16_f32 v68, v68, v69
	v_pk_fma_f32 v[62:63], v[32:33], v[62:63], v[16:17]
	v_cndmask_b32_e32 v46, v46, v48, vcc
	v_rsq_f32_e32 v46, v46
	v_cvt_pk_bf16_f32 v69, v80, v81
	global_store_dwordx2 v[42:43], v[68:69], off offset:-2560
	v_cvt_pk_bf16_f32 v64, v64, v65
	v_mul_f32_e32 v48, 0x45800000, v46
	v_cndmask_b32_e32 v48, v46, v48, vcc
	v_pk_mul_f32 v[58:59], v[48:49], v[58:59] op_sel_hi:[0,1]
	v_pk_mul_f32 v[60:61], v[48:49], v[60:61] op_sel_hi:[0,1]
	v_pk_fma_f32 v[58:59], v[18:19], v[58:59], v[2:3]
	v_cvt_pk_bf16_f32 v65, v62, v63
	global_store_dwordx2 v[42:43], v[64:65], off offset:-2048
	v_pk_fma_f32 v[60:61], v[20:21], v[60:61], v[4:5]
	v_cvt_pk_bf16_f32 v58, v58, v59
	v_mov_b32_e32 v46, v49
	v_cvt_pk_bf16_f32 v59, v60, v61
	global_store_dwordx2 v[42:43], v[58:59], off offset:-1536
	v_mov_b32_e32 v58, v56
	v_mov_b32_e32 v59, v54
	v_pk_mul_f32 v[58:59], v[48:49], v[58:59] op_sel_hi:[0,1]
	v_mov_b32_e32 v54, v57
	v_pk_mul_f32 v[50:51], v[48:49], v[50:51] op_sel_hi:[0,1]
	v_pk_mul_f32 v[46:47], v[48:49], v[46:47] op_sel_hi:[0,1]
	v_pk_mul_f32 v[54:55], v[48:49], v[54:55] op_sel_hi:[0,1]
	v_pk_fma_f32 v[56:57], v[22:23], v[58:59], v[6:7]
	v_pk_mul_f32 v[52:53], v[48:49], v[52:53] op_sel_hi:[0,1]
	v_pk_fma_f32 v[50:51], v[26:27], v[50:51], v[10:11]
	v_pk_mul_f32 v[44:45], v[48:49], v[44:45] op_sel_hi:[0,1]
	v_pk_fma_f32 v[46:47], v[30:31], v[46:47], v[14:15]
	v_pk_fma_f32 v[54:55], v[24:25], v[54:55], v[8:9]
	v_cvt_pk_bf16_f32 v56, v56, v57
	v_pk_fma_f32 v[52:53], v[28:29], v[52:53], v[12:13]
	v_cvt_pk_bf16_f32 v57, v54, v55
	global_store_dwordx2 v[42:43], v[56:57], off offset:-1024
	v_cvt_pk_bf16_f32 v50, v50, v51
	v_cvt_pk_bf16_f32 v51, v52, v53
	global_store_dwordx2 v[42:43], v[50:51], off offset:-512
	v_pk_fma_f32 v[44:45], v[32:33], v[44:45], v[16:17]
	v_cvt_pk_bf16_f32 v46, v46, v47
	s_cmp_lt_i32 s4, s3
	v_cvt_pk_bf16_f32 v47, v44, v45
	global_store_dwordx2 v[42:43], v[46:47], off
	v_lshl_add_u64 v[42:43], v[42:43], 0, s[6:7]
	s_cbranch_scc0 .LBB0_1014
	s_ashr_i32 s9, s4, 31
	s_branch .Lp6_chk
.LBB0_1012:
	v_add_co_u32_e32 v60, vcc, 0xea100000, v42
	s_ashr_i32 s9, s4, 31
	s_nop 0
	v_addc_co_u32_e32 v61, vcc, -1, v43, vcc
	global_load_dwordx2 v[116:117], v[60:61], off offset:-3584
	global_load_dwordx2 v[114:115], v[60:61], off offset:-3072
	global_load_dwordx2 v[112:113], v[60:61], off offset:-2560
	global_load_dwordx2 v[110:111], v[60:61], off offset:-2048
	global_load_dwordx2 v[108:109], v[60:61], off offset:-1536
	global_load_dwordx2 v[106:107], v[60:61], off offset:-1024
	global_load_dwordx2 v[104:105], v[60:61], off offset:-512
	global_load_dwordx2 v[102:103], v[60:61], off
.Lp6_chk:
	s_lshr_b32 s9, s9, 21
	s_add_i32 s9, s4, s9
	s_ashr_i32 s9, s9, 11
	s_cmp_lt_i32 s4, 0x8000
	s_cselect_b32 s9, s9, 16
	s_cmp_eq_u32 s9, s8
	s_cbranch_scc1 .LBB0_1011
	s_mul_i32 s10, s9, 0x6000
	s_mul_hi_i32 s8, s9, 0x6000
	s_add_u32 s10, s77, s10
	s_addc_u32 s11, s82, s8
	s_add_u32 s18, s10, 0x1000
	s_addc_u32 s19, s11, 0
	global_load_dwordx4 v[18:21], v75, s[18:19]
	global_load_dwordx4 v[22:25], v76, s[18:19]
	global_load_dwordx4 v[26:29], v77, s[18:19]
	global_load_dwordx4 v[30:33], v78, s[18:19]
	global_load_dwordx4 v[60:63], v[34:35], off
	global_load_dwordx4 v[64:67], v[36:37], off
	global_load_dwordx4 v[80:83], v[38:39], off
	global_load_dwordx4 v[84:87], v[40:41], off
	global_load_dwordx4 v[2:5], v75, s[10:11]
	global_load_dwordx4 v[6:9], v75, s[10:11] offset:1024
	global_load_dwordx4 v[10:13], v75, s[10:11] offset:2048
	global_load_dwordx4 v[14:17], v75, s[10:11] offset:3072
	s_mov_b32 s8, s9
	s_waitcnt vmcnt(11)
	v_pk_add_f32 v[20:21], v[20:21], 1.0 op_sel_hi:[1,0]
	v_pk_add_f32 v[18:19], v[18:19], 1.0 op_sel_hi:[1,0]
	s_waitcnt vmcnt(10)
	v_pk_add_f32 v[24:25], v[24:25], 1.0 op_sel_hi:[1,0]
	v_pk_add_f32 v[22:23], v[22:23], 1.0 op_sel_hi:[1,0]
	s_waitcnt vmcnt(9)
	v_pk_add_f32 v[28:29], v[28:29], 1.0 op_sel_hi:[1,0]
	v_pk_add_f32 v[26:27], v[26:27], 1.0 op_sel_hi:[1,0]
	s_waitcnt vmcnt(8)
	v_pk_add_f32 v[32:33], v[32:33], 1.0 op_sel_hi:[1,0]
	v_pk_add_f32 v[30:31], v[30:31], 1.0 op_sel_hi:[1,0]
	s_waitcnt vmcnt(7)
	v_pk_mul_f32 v[20:21], v[62:63], v[20:21]
	v_pk_mul_f32 v[18:19], v[60:61], v[18:19]
	s_waitcnt vmcnt(6)
	v_pk_mul_f32 v[24:25], v[66:67], v[24:25]
	v_pk_mul_f32 v[22:23], v[64:65], v[22:23]
	s_waitcnt vmcnt(5)
	v_pk_mul_f32 v[28:29], v[82:83], v[28:29]
	v_pk_mul_f32 v[26:27], v[80:81], v[26:27]
	s_waitcnt vmcnt(4)
	v_pk_mul_f32 v[32:33], v[86:87], v[32:33]
	v_pk_mul_f32 v[30:31], v[84:85], v[30:31]
	s_waitcnt vmcnt(0)
	s_branch .LBB0_1011
